# norm+route: x row and gain vector kept in VGPR rings (rotating), inner loop has no global loads
# speedup vs baseline: 1.0278x; 1.0037x over previous
.LBB0_2066:
	s_or_b64 exec, exec, s[4:5]
	s_lshl_b32 s27, s24, 5
	s_add_i32 s27, s27, s76
	s_add_u32 s29, s22, 0x3df80000
	s_addc_u32 s30, s23, 0
	s_add_u32 s14, s22, 0x8000
	s_addc_u32 s15, s23, 0
	s_add_u32 s31, s22, 0x460000
	s_addc_u32 s33, s23, 0
	s_add_u32 s35, s22, 0x470000
	v_ashrrev_i32_e32 v9, 31, v8
	s_addc_u32 s36, s23, 0
	v_lshlrev_b64 v[2:3], 4, v[8:9]
	s_add_u32 s37, s22, 0x480000
	v_lshl_add_u64 v[22:23], s[6:7], 0, v[2:3]
	s_addc_u32 s38, s23, 0
	v_readlane_b32 s0, v254, 9
	v_readlane_b32 s6, v254, 45
	v_readlane_b32 s1, v254, 10
	s_add_u32 s0, s0, s6
	v_readlane_b32 s6, v254, 46
	s_addc_u32 s1, s1, s6
	v_lshl_add_u64 v[2:3], s[0:1], 0, v[2:3]
	s_mov_b64 s[0:1], 0x2bc80400
	v_lshl_add_u64 v[24:25], v[2:3], 0, s[0:1]
	v_mov_b32_e32 v2, v1
	v_mov_b32_e32 v3, v1
	v_mov_b32_e32 v4, v1
	v_mov_b32_e32 v5, v1
	v_mov_b32_e32 v6, v1
	v_mov_b32_e32 v7, v1
	v_lshlrev_b32_e32 v46, 2, v8
	v_cmp_eq_u32_e64 s[4:5], 0, v8
	v_lshl_add_u32 v49, v8, 4, 0
	v_mov_b32_e32 v0, v1
	v_lshlrev_b64 v[26:27], 2, v[8:9]
	v_mov_b64_e32 v[8:9], v[6:7]
	v_xor_b32_e32 v47, 64, v46
	v_xor_b32_e32 v48, 0x80, v46
	s_mov_b32 s28, 0
	v_mov_b32_e32 v50, 0x358637bd
	s_mov_b32 s39, 0xf800000
	v_mov_b32_e32 v51, 0x260
	s_mov_b32 s40, 0xc3e00000
	s_mov_b64 s[20:21], 0x800
	v_mov_b32_e32 v52, 0x43e00000
	v_mov_b32_e32 v53, 1
	s_mov_b32 s22, s27
	v_mov_b64_e32 v[6:7], v[4:5]
	v_mov_b64_e32 v[4:5], v[2:3]
	v_mov_b64_e32 v[2:3], v[0:1]
	v_lshrrev_b32_e32 v200, 2, v46
	v_lshl_add_u32 v200, s76, 6, v200
	v_lshlrev_b32_e32 v201, 4, v200
	global_load_dwordx4 v[204:207], v201, s[18:19]
	v_add_u32_e32 v202, 0x2000, v201
	global_load_dwordx4 v[208:211], v202, s[18:19]
	v_add_u32_e32 v202, 0x4000, v201
	global_load_dwordx4 v[212:215], v202, s[18:19]
	v_add_u32_e32 v202, 0x6000, v201
	global_load_dwordx4 v[216:219], v202, s[18:19]
	v_add_u32_e32 v202, 0x8000, v201
	global_load_dwordx4 v[220:223], v202, s[18:19]
	v_add_u32_e32 v202, 0xa000, v201
	global_load_dwordx4 v[224:227], v202, s[18:19]
	v_add_u32_e32 v202, 0xc000, v201
	global_load_dwordx4 v[228:231], v202, s[18:19]
	v_add_u32_e32 v202, 0xe000, v201
	global_load_dwordx4 v[232:235], v202, s[18:19]
	v_and_b32_e32 v202, 7, v200
	v_lshrrev_b32_e32 v203, 3, v200
	v_mul_u32_u24_e32 v202, 0x2020, v202
	v_lshl_add_u32 v203, v203, 4, v202
	v_add_u32_e32 v150, 0x4000, v49
	s_waitcnt vmcnt(7)
	ds_write_b128 v203, v[204:207] offset:16384
	s_waitcnt vmcnt(6)
	ds_write_b128 v203, v[208:211] offset:17408
	s_waitcnt vmcnt(5)
	ds_write_b128 v203, v[212:215] offset:18432
	s_waitcnt vmcnt(4)
	ds_write_b128 v203, v[216:219] offset:19456
	s_waitcnt vmcnt(3)
	ds_write_b128 v203, v[220:223] offset:20480
	s_waitcnt vmcnt(2)
	ds_write_b128 v203, v[224:227] offset:21504
	s_waitcnt vmcnt(1)
	ds_write_b128 v203, v[228:231] offset:22528
	s_waitcnt vmcnt(0)
	ds_write_b128 v203, v[232:235] offset:23552
	s_waitcnt lgkmcnt(0)
	s_barrier
	v_add_u32_e32 v152, 0x1000, v49
	global_load_dwordx4 v[188:191], v49, s[16:17]
	global_load_dwordx4 v[192:195], v49, s[16:17] offset:1024
	global_load_dwordx4 v[196:199], v49, s[16:17] offset:2048
	global_load_dwordx4 v[200:203], v49, s[16:17] offset:3072
	global_load_dwordx4 v[204:207], v152, s[16:17]
	global_load_dwordx4 v[208:211], v152, s[16:17] offset:1024
	global_load_dwordx4 v[212:215], v152, s[16:17] offset:2048
	global_load_dwordx4 v[216:219], v152, s[16:17] offset:3072
	s_branch .LBB0_2068

.LBB0_2068:
	s_lshl_b32 s0, s28, 3
	s_add_i32 s24, s27, s0
	s_ashr_i32 s25, s24, 31
	s_lshl_b64 s[0:1], s[24:25], 13
	v_lshl_add_u64 v[32:33], v[22:23], 0, s[0:1]
	global_load_dwordx4 v[156:159], v[32:33], off
	global_load_dwordx4 v[160:163], v[32:33], off offset:1024
	global_load_dwordx4 v[164:167], v[32:33], off offset:2048
	global_load_dwordx4 v[168:171], v[32:33], off offset:3072
	v_add_co_u32_e32 v44, vcc, s26, v32
	s_ashr_i32 s23, s22, 31
	s_nop 0
	v_addc_co_u32_e32 v45, vcc, 0, v33, vcc
	global_load_dwordx4 v[172:175], v[44:45], off
	global_load_dwordx4 v[176:179], v[44:45], off offset:1024
	global_load_dwordx4 v[180:183], v[44:45], off offset:2048
	global_load_dwordx4 v[184:187], v[44:45], off offset:3072
	s_lshl_b64 s[0:1], s[22:23], 13
	s_mov_b64 s[12:13], 1
	s_mov_b32 s25, 0
	s_waitcnt vmcnt(7)
	v_mul_f32_e32 v0, v157, v157
	v_mul_f32_e32 v11, v159, v159
	s_waitcnt vmcnt(6)
	v_mul_f32_e32 v13, v161, v161
	v_mul_f32_e32 v15, v163, v163
	s_waitcnt vmcnt(5)
	v_mul_f32_e32 v17, v165, v165
	v_mul_f32_e32 v19, v167, v167
	v_fmac_f32_e32 v0, v156, v156
	v_fmac_f32_e32 v11, v158, v158
	v_fmac_f32_e32 v13, v160, v160
	v_fmac_f32_e32 v15, v162, v162
	s_waitcnt vmcnt(4)
	v_mul_f32_e32 v21, v169, v169
	v_mul_f32_e32 v29, v171, v171
	v_fmac_f32_e32 v17, v164, v164
	v_fmac_f32_e32 v19, v166, v166
	v_add_f32_e32 v0, v0, v11
	v_add_f32_e32 v11, v13, v15
	v_fmac_f32_e32 v21, v168, v168
	v_fmac_f32_e32 v29, v170, v170
	s_waitcnt vmcnt(3)
	v_mul_f32_e32 v10, v173, v173
	v_mul_f32_e32 v12, v175, v175
	v_add_f32_e32 v13, v17, v19
	v_add_f32_e32 v0, v0, v11
	s_waitcnt vmcnt(2)
	v_mul_f32_e32 v14, v177, v177
	v_mul_f32_e32 v16, v179, v179
	v_add_f32_e32 v15, v21, v29
	v_fmac_f32_e32 v10, v172, v172
	v_fmac_f32_e32 v12, v174, v174
	v_add_f32_e32 v0, v0, v13
	s_waitcnt vmcnt(1)
	v_mul_f32_e32 v18, v181, v181
	v_mul_f32_e32 v20, v183, v183
	v_fmac_f32_e32 v14, v176, v176
	v_fmac_f32_e32 v16, v178, v178
	v_add_f32_e32 v10, v10, v12
	v_add_f32_e32 v0, v0, v15
	s_waitcnt vmcnt(0)
	v_mul_f32_e32 v28, v185, v185
	v_mul_f32_e32 v30, v187, v187
	v_fmac_f32_e32 v18, v180, v180
	v_fmac_f32_e32 v20, v182, v182
	v_add_f32_e32 v11, v14, v16
	v_add_f32_e32 v0, v0, v10
	v_fmac_f32_e32 v28, v184, v184
	v_fmac_f32_e32 v30, v186, v186
	v_add_f32_e32 v12, v18, v20
	v_add_f32_e32 v0, v0, v11
	v_add_f32_e32 v14, v28, v30
	v_add_f32_e32 v0, v0, v12
	v_add_f32_e32 v0, v0, v14
	v_mov_b32_e32 v40, 0
	v_mov_b32_e32 v41, v40
	v_add_f32_dpp v0, v0, v0 quad_perm:[1,0,3,2] row_mask:0xf bank_mask:0xf bound_ctrl:1
	v_mov_b32_e32 v34, v40
	v_mov_b32_e32 v35, v40
	v_add_f32_dpp v0, v0, v0 quad_perm:[2,3,0,1] row_mask:0xf bank_mask:0xf bound_ctrl:1
	v_mov_b32_e32 v30, v40
	v_mov_b32_e32 v31, v40
	v_add_f32_dpp v0, v0, v0 row_half_mirror row_mask:0xf bank_mask:0xf bound_ctrl:1
	v_mov_b32_e32 v28, v40
	v_lshl_add_u64 v[32:33], v[24:25], 0, s[0:1]
	v_add_f32_dpp v10, v0, v0 row_mirror row_mask:0xf bank_mask:0xf bound_ctrl:1
	ds_bpermute_b32 v11, v47, v10
	v_mov_b32_e32 v0, v49
	v_mov_b32_e32 v42, v40
	s_waitcnt lgkmcnt(0)
	v_add_f32_e32 v10, v10, v11
	ds_bpermute_b32 v11, v48, v10
	s_waitcnt lgkmcnt(0)
	v_add_f32_e32 v10, v10, v11
	v_fmamk_f32 v10, v10, 0x3a000000, v50
	v_mul_f32_e32 v11, 0x4f800000, v10
	v_cmp_gt_f32_e32 vcc, s39, v10
	s_nop 1
	v_cndmask_b32_e32 v10, v10, v11, vcc
	v_sqrt_f32_e32 v11, v10
	s_nop 0
	v_add_u32_e32 v12, -1, v11
	v_add_u32_e32 v13, 1, v11
	v_fma_f32 v14, -v12, v11, v10
	v_fma_f32 v15, -v13, v11, v10
	v_cmp_ge_f32_e64 s[6:7], 0, v14
	s_nop 1
	v_cndmask_b32_e64 v11, v11, v12, s[6:7]
	v_cmp_lt_f32_e64 s[6:7], 0, v15
	s_nop 1
	v_cndmask_b32_e64 v11, v11, v13, s[6:7]
	v_mul_f32_e32 v12, 0x37800000, v11
	v_cndmask_b32_e32 v11, v11, v12, vcc
	v_cmp_class_f32_e32 vcc, v10, v51
	s_nop 1
	v_cndmask_b32_e32 v10, v11, v10, vcc
	v_div_scale_f32 v11, s[6:7], v10, v10, 1.0
	v_rcp_f32_e32 v12, v11
	v_div_scale_f32 v13, vcc, 1.0, v10, 1.0
	v_fma_f32 v14, -v11, v12, 1.0
	v_fmac_f32_e32 v12, v14, v12
	v_mul_f32_e32 v14, v13, v12
	v_fma_f32 v15, -v11, v14, v13
	v_fmac_f32_e32 v14, v15, v12
	v_fma_f32 v11, -v11, v14, v13
	v_div_fmas_f32 v11, v11, v12, v14
	v_div_fixup_f32 v37, v11, v10, 1.0
	v_mov_b32_e32 v38, v37
	v_mov_b32_e32 v39, v37
.LBB0_2069:
	v_lshl_add_u32 v151, s25, 2, v150
	ds_read_b128 v[10:13], v0
	ds_read_b128 v[14:17], v0 offset:1024
	ds_read_b128 v[54:57], v0 offset:8192
	ds_read_b128 v[58:61], v0 offset:9216
	v_mov_b64_e32 v[62:63], v[156:157]
	v_mov_b64_e32 v[64:65], v[158:159]
	v_mov_b64_e32 v[18:19], v[160:161]
	v_mov_b64_e32 v[20:21], v[162:163]
	v_mov_b64_e32 v[156:157], v[164:165]
	v_mov_b64_e32 v[158:159], v[166:167]
	v_mov_b64_e32 v[160:161], v[168:169]
	v_mov_b64_e32 v[162:163], v[170:171]
	v_mov_b64_e32 v[164:165], v[172:173]
	v_mov_b64_e32 v[166:167], v[174:175]
	v_mov_b64_e32 v[168:169], v[176:177]
	v_mov_b64_e32 v[170:171], v[178:179]
	v_mov_b64_e32 v[172:173], v[180:181]
	v_mov_b64_e32 v[174:175], v[182:183]
	v_mov_b64_e32 v[176:177], v[184:185]
	v_mov_b64_e32 v[178:179], v[186:187]
	v_mov_b64_e32 v[66:67], v[188:189]
	v_mov_b64_e32 v[68:69], v[190:191]
	ds_read_b128 v[70:73], v151 offset:8224
	ds_read_b128 v[74:77], v151 offset:0
	v_mov_b64_e32 v[78:79], v[192:193]
	v_mov_b64_e32 v[80:81], v[194:195]
	v_mov_b64_e32 v[188:189], v[196:197]
	v_mov_b64_e32 v[190:191], v[198:199]
	v_mov_b64_e32 v[192:193], v[200:201]
	v_mov_b64_e32 v[194:195], v[202:203]
	v_mov_b64_e32 v[196:197], v[204:205]
	v_mov_b64_e32 v[198:199], v[206:207]
	v_mov_b64_e32 v[200:201], v[208:209]
	v_mov_b64_e32 v[202:203], v[210:211]
	v_mov_b64_e32 v[204:205], v[212:213]
	v_mov_b64_e32 v[206:207], v[214:215]
	v_mov_b64_e32 v[208:209], v[216:217]
	v_mov_b64_e32 v[210:211], v[218:219]
	v_mov_b64_e32 v[212:213], v[66:67]
	v_mov_b64_e32 v[214:215], v[68:69]
	v_mov_b64_e32 v[216:217], v[78:79]
	v_mov_b64_e32 v[218:219], v[80:81]
	ds_read_b128 v[82:85], v151 offset:41120
	ds_read_b128 v[86:89], v151 offset:57568
	ds_read_b128 v[90:93], v151 offset:9248
	ds_read_b128 v[94:97], v151 offset:42144
	ds_read_b128 v[98:101], v151 offset:58592
	ds_read_b128 v[102:105], v151 offset:16448
	ds_read_b128 v[106:109], v151 offset:24672
	ds_read_b128 v[110:113], v151 offset:32896
	ds_read_b128 v[114:117], v151 offset:1024
	s_waitcnt lgkmcnt(14)
	ds_read_b128 v[118:121], v151 offset:33920
	s_waitcnt lgkmcnt(13)
	v_add_f32_e32 v36, 1.0, v54
	ds_read_b128 v[122:125], v151 offset:49344
	v_add_f32_e32 v45, 1.0, v55
	v_pk_add_f32 v[134:135], v[56:57], 1.0 op_sel_hi:[1,0]
	ds_read_b128 v[54:57], v151 offset:25696
	s_waitcnt lgkmcnt(14)
	ds_read_b128 v[126:129], v151 offset:17472
	s_waitcnt lgkmcnt(14)
	ds_read_b128 v[130:133], v151 offset:50368
	v_mov_b32_e32 v43, v11
	v_mov_b32_e32 v136, v14
	s_waitcnt lgkmcnt(15)
	v_pk_add_f32 v[60:61], v[60:61], 1.0 op_sel_hi:[1,0]
	v_mov_b32_e32 v142, 0
	v_add_f32_e32 v59, 1.0, v59
	s_add_i32 s23, s12, -1
	s_cmp_eq_u32 s23, 0
	s_cselect_b64 vcc, -1, 0
	s_cmp_eq_u32 s23, 1
	v_mov_b32_e32 v143, 0
	s_cselect_b64 s[6:7], -1, 0
	s_cmp_eq_u32 s23, 2
	s_cselect_b64 s[8:9], -1, 0
	s_cmp_eq_u32 s23, 3
	s_cselect_b64 s[10:11], -1, 0
	s_cmp_eq_u32 s23, 4
	v_lshl_add_u64 v[32:33], v[32:33], 0, s[20:21]
	v_add_u32_e32 v0, 0x800, v0
	v_mul_f32_e32 v11, v37, v62
	v_pk_mul_f32 v[64:65], v[38:39], v[64:65]
	v_mov_b32_e32 v139, v63
	v_pk_mul_f32 v[62:63], v[36:37], v[62:63]
	v_mul_f32_e32 v14, v37, v18
	v_pk_mul_f32 v[20:21], v[38:39], v[20:21]
	v_mov_b32_e32 v141, v19
	v_mul_f32_e32 v138, v66, v11
	v_mov_b32_e32 v11, v67
	v_pk_mul_f32 v[64:65], v[68:69], v[64:65]
	v_pk_mul_f32 v[62:63], v[66:67], v[62:63]
	v_pk_fma_f32 v[10:11], v[36:37], v[138:139], v[10:11]
	v_pk_fma_f32 v[12:13], v[134:135], v[64:65], v[12:13]
	v_mov_b32_e32 v62, v10
	v_add_f32_e32 v36, 1.0, v58
	v_pk_mul_f32 v[18:19], v[36:37], v[18:19]
	s_waitcnt lgkmcnt(15)
	v_mov_b32_e32 v44, v73
	s_waitcnt lgkmcnt(14)
	v_pk_fma_f32 v[40:41], v[74:75], v[10:11], v[40:41] op_sel_hi:[1,0,1]
	s_waitcnt lgkmcnt(14)
	v_mul_f32_e32 v140, v78, v14
	v_pk_mul_f32 v[20:21], v[80:81], v[20:21]
	v_cvt_pk_bf16_f32 v14, v12, v13
	v_mov_b32_e32 v137, v79
	s_waitcnt lgkmcnt(13)
	v_mov_b32_e32 v66, v85
	s_waitcnt lgkmcnt(12)
	v_mov_b32_e32 v67, v89
	v_pk_fma_f32 v[16:17], v[60:61], v[20:21], v[16:17]
	v_pk_fma_f32 v[42:43], v[44:45], v[62:63], v[42:43]
	v_lshlrev_b32_e32 v29, 16, v14
	v_fmac_f32_e32 v28, v72, v10
	v_pk_fma_f32 v[34:35], v[76:77], v[10:11], v[34:35] op_sel_hi:[1,0,1]
	v_pk_fma_f32 v[30:31], v[70:71], v[10:11], v[30:31] op_sel_hi:[1,0,1]
	v_pk_fma_f32 v[70:71], v[36:37], v[140:141], v[136:137]
	s_waitcnt lgkmcnt(10)
	v_mov_b32_e32 v20, v97
	s_waitcnt lgkmcnt(9)
	v_mov_b32_e32 v21, v101
	v_and_b32_e32 v14, 0xffff0000, v14
	v_pk_mul_f32 v[44:45], v[12:13], v[66:67]
	v_cvt_pk_bf16_f32 v36, v16, v17
	v_cvt_pk_bf16_f32 v66, v10, v43
	s_waitcnt lgkmcnt(8)
	v_pk_fma_f32 v[10:11], v[42:43], v[102:103], v[40:41] op_sel:[1,0,0]
	v_mul_f32_e32 v40, 0x41800000, v29
	v_mov_b32_e32 v29, v42
	v_mul_f32_e32 v64, v12, v84
	v_pk_mul_f32 v[20:21], v[16:17], v[20:21]
	v_pk_fma_f32 v[34:35], v[42:43], v[104:105], v[34:35] op_sel:[1,0,0]
	s_waitcnt lgkmcnt(7)
	v_pk_fma_f32 v[30:31], v[42:43], v[106:107], v[30:31] op_sel:[1,0,0]
	v_mov_b32_e32 v65, v44
	v_mov_b32_e32 v69, v45
	v_mul_f32_e32 v14, 0x41800000, v14
	v_lshlrev_b32_e32 v41, 16, v36
	v_and_b32_e32 v36, 0xffff0000, v36
	v_lshlrev_b32_e32 v44, 16, v66
	v_and_b32_e32 v45, 0xffff0000, v66
	v_pk_fma_f32 v[28:29], v[42:43], v[108:109], v[28:29] op_sel:[1,0,0]
	v_mul_f32_e32 v68, v13, v88
	v_mov_b32_e32 v61, v20
	v_mov_b32_e32 v63, v21
	s_waitcnt lgkmcnt(6)
	v_pk_fma_f32 v[10:11], v[12:13], v[110:111], v[10:11] op_sel_hi:[0,1,1]
	v_pk_fma_f32 v[20:21], v[12:13], v[112:113], v[34:35] op_sel_hi:[0,1,1]
	v_pk_fma_f32 v[30:31], v[12:13], v[82:83], v[30:31] op_sel_hi:[0,1,1]
	v_med3_f32 v34, v14, s40, v52
	v_mul_f32_e32 v14, 0x41800000, v41
	v_mul_f32_e32 v35, 0x41800000, v36
	v_mul_f32_e32 v36, 0x41800000, v44
	v_mul_f32_e32 v41, 0x41800000, v45
	v_pk_add_f32 v[28:29], v[28:29], v[64:65]
	v_pk_mul_f32 v[18:19], v[78:79], v[18:19]
	s_waitcnt lgkmcnt(3)
	v_pk_fma_f32 v[10:11], v[12:13], v[122:123], v[10:11] op_sel:[1,0,0]
	v_pk_fma_f32 v[20:21], v[12:13], v[124:125], v[20:21] op_sel:[1,0,0]
	v_pk_fma_f32 v[12:13], v[12:13], v[86:87], v[30:31] op_sel:[1,0,0]
	v_med3_f32 v43, v14, s40, v52
	v_med3_f32 v14, v36, s40, v52
	v_med3_f32 v30, v41, s40, v52
	v_pk_add_f32 v[28:29], v[28:29], v[68:69]
	v_mov_b32_e32 v58, v93
	v_mov_b32_e32 v18, v70
	v_cvt_pk_fp8_f32 v142, v14, v30
	v_mov_b32_e32 v14, v29
	v_pk_fma_f32 v[14:15], v[58:59], v[18:19], v[14:15]
	v_pk_fma_f32 v[20:21], v[116:117], v[70:71], v[20:21] op_sel_hi:[1,0,1]
	v_pk_fma_f32 v[12:13], v[90:91], v[70:71], v[12:13] op_sel_hi:[1,0,1]
	v_cvt_pk_bf16_f32 v30, v70, v15
	v_med3_f32 v40, v40, s40, v52
	s_waitcnt lgkmcnt(1)
	v_pk_fma_f32 v[18:19], v[14:15], v[128:129], v[20:21] op_sel:[1,0,0]
	v_pk_fma_f32 v[12:13], v[14:15], v[54:55], v[12:13] op_sel:[1,0,0]
	v_lshlrev_b32_e32 v20, 16, v30
	v_and_b32_e32 v21, 0xffff0000, v30
	v_pk_fma_f32 v[12:13], v[16:17], v[94:95], v[12:13] op_sel_hi:[0,1,1]
	v_cvt_pk_fp8_f32 v142, v40, v34 op_sel:[0,0,1]
	v_mul_f32_e32 v20, 0x41800000, v20
	v_mul_f32_e32 v21, 0x41800000, v21
	v_pk_fma_f32 v[30:31], v[16:17], v[98:99], v[12:13] op_sel:[1,0,0]
	v_med3_f32 v12, v20, s40, v52
	v_med3_f32 v13, v21, s40, v52
	v_cvt_pk_fp8_f32 v143, v12, v13
	v_cndmask_b32_e32 v2, v2, v142, vcc
	s_cselect_b64 vcc, -1, 0
	s_cmp_eq_u32 s23, 5
	v_med3_f32 v44, v35, s40, v52
	v_cndmask_b32_e32 v6, v6, v142, vcc
	s_cselect_b64 vcc, -1, 0
	s_cmp_eq_u32 s23, 6
	v_cndmask_b32_e32 v7, v7, v142, vcc
	s_cselect_b64 vcc, -1, 0
	s_cmp_eq_u32 s23, 7
	v_cvt_pk_fp8_f32 v143, v43, v44 op_sel:[0,0,1]
	v_cndmask_b32_e32 v8, v8, v142, vcc
	s_cselect_b64 vcc, -1, 0
	s_cmp_eq_u32 s12, 7
	v_cndmask_b32_e32 v9, v9, v142, vcc
	s_cselect_b64 vcc, -1, 0
	s_cmp_eq_u32 s12, 6
	v_cndmask_b32_e64 v3, v3, v142, s[6:7]
	s_cselect_b64 s[6:7], -1, 0
	s_cmp_eq_u32 s12, 5
	v_cndmask_b32_e32 v9, v9, v143, vcc
	s_cselect_b64 vcc, -1, 0
	s_cmp_eq_u32 s12, 4
	v_cndmask_b32_e32 v7, v7, v143, vcc
	s_cselect_b64 vcc, -1, 0
	s_cmp_eq_u32 s12, 3
	v_cndmask_b32_e64 v5, v5, v142, s[10:11]
	v_cndmask_b32_e32 v6, v6, v143, vcc
	s_cselect_b64 vcc, -1, 0
	s_cmp_eq_u32 s12, 2
	v_pk_fma_f32 v[10:11], v[114:115], v[70:71], v[10:11] op_sel_hi:[1,0,1]
	v_cndmask_b32_e64 v4, v4, v142, s[8:9]
	v_cndmask_b32_e32 v5, v5, v143, vcc
	s_cselect_b64 vcc, -1, 0
	s_cmp_eq_u32 s12, 1
	v_fmac_f32_e32 v28, v92, v70
	v_pk_fma_f32 v[10:11], v[14:15], v[126:127], v[10:11] op_sel:[1,0,0]
	v_mov_b32_e32 v29, v14
	v_cndmask_b32_e32 v4, v4, v143, vcc
	s_cselect_b64 vcc, -1, 0
	s_cmp_eq_u32 s12, 0
	v_mul_f32_e32 v60, v16, v96
	v_pk_fma_f32 v[10:11], v[16:17], v[118:119], v[10:11] op_sel_hi:[0,1,1]
	v_pk_fma_f32 v[14:15], v[14:15], v[56:57], v[28:29] op_sel:[1,0,0]
	v_cndmask_b32_e32 v3, v3, v143, vcc
	s_cselect_b64 vcc, -1, 0
	s_addk_i32 s25, 0x200
	v_mul_f32_e32 v62, v17, v100
	s_waitcnt lgkmcnt(0)
	v_pk_fma_f32 v[40:41], v[16:17], v[130:131], v[10:11] op_sel:[1,0,0]
	v_pk_add_f32 v[10:11], v[14:15], v[60:61]
	s_add_u32 s12, s12, 2
	v_pk_fma_f32 v[18:19], v[16:17], v[120:121], v[18:19] op_sel_hi:[0,1,1]
	v_pk_add_f32 v[28:29], v[10:11], v[62:63]
	s_addc_u32 s13, s13, 0
	v_pk_fma_f32 v[34:35], v[16:17], v[132:133], v[18:19] op_sel:[1,0,0]
	v_mov_b32_e32 v42, v29
	v_cndmask_b32_e64 v8, v8, v143, s[6:7]
	s_cmpk_eq_i32 s25, 0x800
	v_cndmask_b32_e32 v2, v2, v143, vcc
	s_cbranch_scc0 .LBB0_2069
	v_mov_b32_dpp v10, v40 quad_perm:[1,0,3,2] row_mask:0xf bank_mask:0xf bound_ctrl:1
	v_mov_b32_dpp v11, v41 quad_perm:[1,0,3,2] row_mask:0xf bank_mask:0xf bound_ctrl:1
	v_pk_add_f32 v[10:11], v[40:41], v[10:11]
	v_add_f32_dpp v0, v34, v34 quad_perm:[1,0,3,2] row_mask:0xf bank_mask:0xf bound_ctrl:1
	v_add_f32_dpp v15, v35, v35 quad_perm:[1,0,3,2] row_mask:0xf bank_mask:0xf bound_ctrl:1
	v_mov_b32_dpp v12, v10 quad_perm:[2,3,0,1] row_mask:0xf bank_mask:0xf bound_ctrl:1
	v_mov_b32_dpp v13, v11 quad_perm:[2,3,0,1] row_mask:0xf bank_mask:0xf bound_ctrl:1
	v_pk_add_f32 v[10:11], v[10:11], v[12:13]
	v_add_f32_dpp v0, v0, v0 quad_perm:[2,3,0,1] row_mask:0xf bank_mask:0xf bound_ctrl:1
	v_add_f32_dpp v15, v15, v15 quad_perm:[2,3,0,1] row_mask:0xf bank_mask:0xf bound_ctrl:1
	v_mov_b32_dpp v12, v10 row_half_mirror row_mask:0xf bank_mask:0xf bound_ctrl:1
	v_mov_b32_dpp v13, v11 row_half_mirror row_mask:0xf bank_mask:0xf bound_ctrl:1
	v_add_f32_dpp v0, v0, v0 row_half_mirror row_mask:0xf bank_mask:0xf bound_ctrl:1
	v_pk_add_f32 v[10:11], v[10:11], v[12:13]
	v_add_f32_dpp v15, v15, v15 row_half_mirror row_mask:0xf bank_mask:0xf bound_ctrl:1
	v_add_f32_dpp v0, v0, v0 row_mirror row_mask:0xf bank_mask:0xf bound_ctrl:1
	v_mov_b32_dpp v12, v10 row_mirror row_mask:0xf bank_mask:0xf bound_ctrl:1
	v_mov_b32_dpp v13, v11 row_mirror row_mask:0xf bank_mask:0xf bound_ctrl:1
	ds_bpermute_b32 v14, v47, v0
	v_pk_add_f32 v[10:11], v[10:11], v[12:13]
	ds_bpermute_b32 v12, v47, v10
	ds_bpermute_b32 v13, v47, v11
	v_add_f32_dpp v16, v30, v30 quad_perm:[1,0,3,2] row_mask:0xf bank_mask:0xf bound_ctrl:1
	s_waitcnt lgkmcnt(2)
	v_add_f32_e32 v0, v0, v14
	ds_bpermute_b32 v14, v48, v0
	v_add_f32_dpp v15, v15, v15 row_mirror row_mask:0xf bank_mask:0xf bound_ctrl:1
	s_waitcnt lgkmcnt(1)
	v_pk_add_f32 v[10:11], v[10:11], v[12:13]
	v_add_f32_dpp v16, v16, v16 quad_perm:[2,3,0,1] row_mask:0xf bank_mask:0xf bound_ctrl:1
	ds_bpermute_b32 v12, v48, v10
	ds_bpermute_b32 v13, v48, v11
	ds_bpermute_b32 v18, v47, v15
	v_add_f32_dpp v16, v16, v16 row_half_mirror row_mask:0xf bank_mask:0xf bound_ctrl:1
	s_waitcnt lgkmcnt(3)
	v_add_f32_e32 v0, v0, v14
	v_add_f32_dpp v14, v31, v31 quad_perm:[1,0,3,2] row_mask:0xf bank_mask:0xf bound_ctrl:1
	v_add_f32_dpp v19, v16, v16 row_mirror row_mask:0xf bank_mask:0xf bound_ctrl:1
	ds_bpermute_b32 v20, v47, v19
	v_add_f32_dpp v14, v14, v14 quad_perm:[2,3,0,1] row_mask:0xf bank_mask:0xf bound_ctrl:1
	s_waitcnt lgkmcnt(2)
	v_pk_add_f32 v[16:17], v[10:11], v[12:13]
	s_waitcnt lgkmcnt(1)
	v_add_f32_e32 v10, v15, v18
	v_add_f32_dpp v14, v14, v14 row_half_mirror row_mask:0xf bank_mask:0xf bound_ctrl:1
	v_add_f32_dpp v18, v28, v28 quad_perm:[1,0,3,2] row_mask:0xf bank_mask:0xf bound_ctrl:1
	ds_bpermute_b32 v11, v48, v10
	v_add_f32_dpp v14, v14, v14 row_mirror row_mask:0xf bank_mask:0xf bound_ctrl:1
	v_add_f32_dpp v18, v18, v18 quad_perm:[2,3,0,1] row_mask:0xf bank_mask:0xf bound_ctrl:1
	s_waitcnt lgkmcnt(1)
	v_add_f32_e32 v12, v19, v20
	ds_bpermute_b32 v15, v47, v14
	v_add_f32_dpp v18, v18, v18 row_half_mirror row_mask:0xf bank_mask:0xf bound_ctrl:1
	v_add_f32_dpp v20, v29, v29 quad_perm:[1,0,3,2] row_mask:0xf bank_mask:0xf bound_ctrl:1
	ds_bpermute_b32 v13, v48, v12
	v_add_f32_dpp v18, v18, v18 row_mirror row_mask:0xf bank_mask:0xf bound_ctrl:1
	v_add_f32_dpp v20, v20, v20 quad_perm:[2,3,0,1] row_mask:0xf bank_mask:0xf bound_ctrl:1
	ds_bpermute_b32 v19, v47, v18
	v_cmp_gt_f32_e64 s[6:7], v17, v16
	v_add_f32_dpp v20, v20, v20 row_half_mirror row_mask:0xf bank_mask:0xf bound_ctrl:1
	s_waitcnt lgkmcnt(2)
	v_add_f32_e32 v14, v14, v15
	v_add_f32_e32 v11, v10, v11
	v_add_f32_dpp v20, v20, v20 row_mirror row_mask:0xf bank_mask:0xf bound_ctrl:1
	ds_bpermute_b32 v21, v47, v20
	v_cndmask_b32_e64 v10, v16, v17, s[6:7]
	ds_bpermute_b32 v15, v48, v14
	v_cmp_gt_f32_e32 vcc, v0, v10
	s_waitcnt lgkmcnt(2)
	v_add_f32_e32 v18, v18, v19
	v_add_f32_e32 v28, v12, v13
	v_cndmask_b32_e64 v12, 0, 1, s[6:7]
	v_cndmask_b32_e32 v10, v10, v0, vcc
	ds_bpermute_b32 v19, v48, v18
	v_cndmask_b32_e64 v12, v12, 2, vcc
	v_cmp_gt_f32_e32 vcc, v11, v10
	s_waitcnt lgkmcnt(2)
	v_add_f32_e32 v20, v20, v21
	ds_bpermute_b32 v21, v48, v20
	v_cndmask_b32_e32 v10, v10, v11, vcc
	v_cndmask_b32_e64 v12, v12, 3, vcc
	v_cmp_gt_f32_e32 vcc, v28, v10
	s_waitcnt lgkmcnt(2)
	v_add_f32_e32 v15, v14, v15
	s_waitcnt lgkmcnt(1)
	v_add_f32_e32 v18, v18, v19
	v_cndmask_b32_e32 v10, v10, v28, vcc
	v_cndmask_b32_e64 v12, v12, 4, vcc
	v_cmp_gt_f32_e32 vcc, v15, v10
	s_waitcnt lgkmcnt(0)
	v_add_f32_e32 v13, v20, v21
	v_cndmask_b32_e32 v10, v10, v15, vcc
	v_cmp_gt_f32_e64 s[8:9], v18, v10
	v_cndmask_b32_e64 v12, v12, 5, vcc
	s_nop 0
	v_cndmask_b32_e64 v14, v10, v18, s[8:9]
	v_cndmask_b32_e64 v10, v12, 6, s[8:9]
	v_cmp_ngt_f32_e32 vcc, v13, v14
	v_mov_b32_e32 v12, 0
	s_nop 0
	v_cndmask_b32_e32 v10, 7, v10, vcc
	v_cmp_eq_u32_e64 s[10:11], 0, v10
	v_cmp_ne_u32_e64 s[12:13], 1, v10
	s_or_b64 s[0:1], s[10:11], s[6:7]
	s_and_b64 s[6:7], s[12:13], s[0:1]
	v_cndmask_b32_e64 v16, v16, v17, s[6:7]
	v_cndmask_b32_e64 v19, 0, 1, s[6:7]
	v_cmp_gt_f32_e64 s[6:7], v0, v16
	s_nop 1
	v_cndmask_b32_e64 v17, v19, 2, s[6:7]
	v_cndmask_b32_e64 v0, v16, v0, s[6:7]
	v_cmp_eq_u32_e64 s[6:7], 2, v10
	s_nop 1
	v_cndmask_b32_e64 v16, v0, v16, s[6:7]
	v_cndmask_b32_e64 v19, v17, v19, s[6:7]
	v_cmp_gt_f32_e64 s[6:7], v11, v16
	s_nop 1
	v_cndmask_b32_e64 v19, v19, 3, s[6:7]
	v_cndmask_b32_e64 v11, v16, v11, s[6:7]
	v_cmp_eq_u32_e64 s[6:7], 3, v10
	s_nop 1
	v_cndmask_b32_e64 v0, v11, v0, s[6:7]
	v_cndmask_b32_e64 v16, v19, v17, s[6:7]
	v_cmp_gt_f32_e64 s[6:7], v28, v0
	s_nop 1
	v_cndmask_b32_e64 v16, v16, 4, s[6:7]
	v_cndmask_b32_e64 v0, v0, v28, s[6:7]
	v_cmp_eq_u32_e64 s[6:7], 4, v10
	s_nop 1
	v_cndmask_b32_e64 v11, v0, v11, s[6:7]
	v_cndmask_b32_e64 v17, v16, v19, s[6:7]
	v_cmp_gt_f32_e64 s[6:7], v15, v11
	s_nop 1
	v_cndmask_b32_e64 v17, v17, 5, s[6:7]
	v_cndmask_b32_e64 v11, v11, v15, s[6:7]
	v_cmp_eq_u32_e64 s[6:7], 5, v10
	s_nop 1
	v_cndmask_b32_e64 v0, v11, v0, s[6:7]
	v_cndmask_b32_e64 v15, v17, v16, s[6:7]
	v_cmp_gt_f32_e64 s[6:7], v18, v0
	s_nop 1
	v_cndmask_b32_e64 v11, v15, 6, s[6:7]
	v_cndmask_b32_e64 v16, v0, v18, s[6:7]
	s_and_b64 s[6:7], s[8:9], vcc
	v_cndmask_b32_e64 v17, v11, v15, s[6:7]
	v_cndmask_b32_e64 v15, v16, v0, s[6:7]
	v_cmp_gt_f32_e64 s[6:7], v13, v15
	s_nop 1
	v_cndmask_b32_e64 v0, v17, 7, s[6:7]
	v_cndmask_b32_e32 v11, v11, v0, vcc
	v_mov_b32_e32 v0, 0
	s_and_saveexec_b64 s[8:9], s[4:5]
	s_cbranch_execz .LBB0_2067
	v_lshlrev_b32_e32 v0, 6, v10
	v_lshl_add_u64 v[16:17], v[0:1], 2, s[14:15]
	v_lshlrev_b32_e32 v0, 6, v11
	global_atomic_add v12, v[16:17], v53, off sc0
	v_lshl_add_u64 v[16:17], v[0:1], 2, s[14:15]
	global_atomic_add v0, v[16:17], v53, off sc0
	s_and_b64 s[6:7], vcc, s[6:7]
	v_cndmask_b32_e64 v15, v15, v13, s[6:7]
	v_cndmask_b32_e32 v13, v13, v14, vcc
	v_sub_f32_e32 v13, v15, v13
	v_mul_f32_e32 v13, 0x3fb8aa3b, v13
	s_lshl_b32 s0, s24, 1
	v_exp_f32_e32 v13, v13
	s_ashr_i32 s1, s0, 31
	s_lshl_b64 s[10:11], s[0:1], 2
	s_add_u32 s6, s31, s10
	s_addc_u32 s7, s33, s11
	v_add_f32_e32 v14, 1.0, v13
	global_store_dwordx2 v1, v[10:11], s[6:7]
	v_div_scale_f32 v15, s[6:7], v14, v14, 1.0
	v_div_scale_f32 v17, s[6:7], v14, v14, v13
	v_rcp_f32_e32 v19, v15
	v_rcp_f32_e32 v20, v17
	s_or_b32 s0, s0, 1
	s_ashr_i32 s1, s0, 31
	v_fma_f32 v21, -v15, v19, 1.0
	s_add_u32 s12, s35, s10
	v_div_scale_f32 v16, vcc, 1.0, v14, 1.0
	v_fma_f32 v28, -v17, v20, 1.0
	v_fmac_f32_e32 v19, v21, v19
	s_addc_u32 s13, s36, s11
	s_lshl_b64 s[0:1], s[0:1], 2
	v_div_scale_f32 v18, s[6:7], v13, v14, v13
	v_fmac_f32_e32 v20, v28, v20
	v_mul_f32_e32 v21, v16, v19
	s_add_u32 s24, s35, s0
	v_mul_f32_e32 v28, v18, v20
	v_fma_f32 v29, -v15, v21, v16
	s_addc_u32 s25, s36, s1
	v_fma_f32 v30, -v17, v28, v18
	v_fmac_f32_e32 v21, v29, v19
	s_add_u32 s10, s37, s10
	v_fmac_f32_e32 v28, v30, v20
	v_fma_f32 v15, -v15, v21, v16
	s_addc_u32 s11, s38, s11
	v_fma_f32 v16, -v17, v28, v18
	v_div_fmas_f32 v15, v15, v19, v21
	s_mov_b64 vcc, s[6:7]
	s_add_u32 s0, s37, s0
	v_div_fixup_f32 v15, v15, v14, 1.0
	v_div_fmas_f32 v16, v16, v20, v28
	s_addc_u32 s1, s38, s1
	v_div_fixup_f32 v13, v16, v14, v13
	global_store_dword v1, v15, s[10:11]
	s_waitcnt vmcnt(3)
	global_store_dword v1, v12, s[12:13]
	s_waitcnt vmcnt(3)
	global_store_dword v1, v0, s[24:25]
	global_store_dword v1, v13, s[0:1]
	s_branch .LBB0_2067
